# H1 stage 2: eight transposed-read MFMA steps software-pipelined (LDS reads 3 steps ahead through a ring of 4 register sets in v[152:183], MFMA result latency overlapped with the next step)
# speedup vs baseline: 1.0053x; 1.0013x over previous
.LBB0_564:
	s_waitcnt lgkmcnt(0)
	s_barrier
	ds_read_b64_tr_b16 v[16:17], v131
	ds_read_b64_tr_b16 v[18:19], v131 offset:1088
	ds_read_b64_tr_b16 v[12:13], v131 offset:8704
	ds_read_b64_tr_b16 v[14:15], v131 offset:9792
	ds_read_b128 v[20:23], v132
	s_mov_b32 s39, 0x10000
	v_add_u32_e32 v59, v114, v115
	s_waitcnt vmcnt(24)
	v_mov_b32_e32 v100, v134
	s_waitcnt vmcnt(22)
	v_mov_b32_e32 v148, v135
	s_waitcnt lgkmcnt(0)
	v_mfma_f32_16x16x32_bf16 v[20:23], v[16:19], v[20:23], 0
	s_waitcnt vmcnt(20)
	v_mov_b32_e32 v147, v136
	s_waitcnt vmcnt(18)
	v_mov_b32_e32 v146, v137
	s_waitcnt vmcnt(16)
	v_mov_b32_e32 v145, v138
	s_waitcnt vmcnt(14)
	v_mov_b32_e32 v144, v139
	s_waitcnt vmcnt(13)
	v_mov_b32_e32 v143, v140
	v_cvt_pk_bf16_f32 v20, v20, v21
	v_cvt_pk_bf16_f32 v21, v22, v23
	v_lshl_add_u64 v[22:23], s[78:79], 1, v[54:55]
	v_lshl_add_u64 v[22:23], s[54:55], 1, v[22:23]
	v_lshl_add_u64 v[60:61], v[22:23], 0, v[2:3]
	global_store_dwordx2 v[60:61], v[20:21], off
	ds_read_b128 v[20:23], v132 offset:2304
	ds_read_b128 v[24:27], v132 offset:4672
	s_waitcnt lgkmcnt(1)
	v_mfma_f32_16x16x32_bf16 v[20:23], v[16:19], v[20:23], 0
	v_readlane_b32 s78, v250, 1
	s_waitcnt vmcnt(12)
	v_mov_b32_e32 v142, v141
	s_mov_b32 s82, s81
	s_nop 3
	v_cvt_pk_bf16_f32 v20, v20, v21
	v_cvt_pk_bf16_f32 v21, v22, v23
	v_add_co_u32_e32 v22, vcc, s39, v60
	s_mov_b32 s39, 0x20000
	s_nop 0
	v_addc_co_u32_e32 v23, vcc, 0, v61, vcc
	global_store_dwordx2 v[22:23], v[20:21], off
	ds_read_b128 v[20:23], v132 offset:4608
	s_waitcnt lgkmcnt(0)
	v_mfma_f32_16x16x32_bf16 v[20:23], v[16:19], v[20:23], 0
	v_readlane_b32 s79, v250, 2
	v_mfma_f32_16x16x32_bf16 v[20:23], v[12:15], v[24:27], v[20:23]
	ds_read_b128 v[24:27], v132 offset:6976
	s_nop 6
	v_cvt_pk_bf16_f32 v20, v20, v21
	v_cvt_pk_bf16_f32 v21, v22, v23
	v_add_co_u32_e32 v22, vcc, s39, v60
	s_mov_b32 s39, 0x30000
	s_nop 0
	v_addc_co_u32_e32 v23, vcc, 0, v61, vcc
	global_store_dwordx2 v[22:23], v[20:21], off
	ds_read_b128 v[20:23], v132 offset:6912
	s_waitcnt lgkmcnt(0)
	v_mfma_f32_16x16x32_bf16 v[20:23], v[16:19], v[20:23], 0
	v_mfma_f32_16x16x32_bf16 v[20:23], v[12:15], v[24:27], v[20:23]
	s_nop 7
	v_cvt_pk_bf16_f32 v20, v20, v21
	v_cvt_pk_bf16_f32 v21, v22, v23
	v_add_co_u32_e32 v22, vcc, s39, v60
	s_ashr_i32 s39, s38, 31
	s_nop 0
	v_addc_co_u32_e32 v23, vcc, 0, v61, vcc
	global_store_dwordx2 v[22:23], v[20:21], off
	ds_read_b64_tr_b16 v[152:153], v59 offset:60928
	ds_read_b64_tr_b16 v[154:155], v59 offset:62016
	ds_read_b64_tr_b16 v[156:157], v133 offset:60928
	ds_read_b64_tr_b16 v[158:159], v133 offset:62016
	ds_read_b64_tr_b16 v[160:161], v59 offset:60960
	ds_read_b64_tr_b16 v[162:163], v59 offset:62048
	ds_read_b64_tr_b16 v[164:165], v133 offset:60960
	ds_read_b64_tr_b16 v[166:167], v133 offset:62048
	ds_read_b64_tr_b16 v[168:169], v59 offset:60992
	ds_read_b64_tr_b16 v[170:171], v59 offset:62080
	ds_read_b64_tr_b16 v[172:173], v133 offset:60992
	ds_read_b64_tr_b16 v[174:175], v133 offset:62080
	s_lshl_b64 s[38:39], s[38:39], 15
	s_and_b64 vcc, exec, s[76:77]
	v_lshl_add_u64 v[20:21], v[56:57], 0, s[38:39]
	s_waitcnt lgkmcnt(8)
	v_mfma_f32_16x16x32_bf16 v[152:155], v[152:155], v[16:19], 0
	v_mfma_f32_16x16x32_bf16 v[152:155], v[156:159], v[12:15], v[152:155]
	ds_read_b64_tr_b16 v[176:177], v59 offset:61024
	ds_read_b64_tr_b16 v[178:179], v59 offset:62112
	ds_read_b64_tr_b16 v[180:181], v133 offset:61024
	ds_read_b64_tr_b16 v[182:183], v133 offset:62112
	s_waitcnt lgkmcnt(8)
	v_mfma_f32_16x16x32_bf16 v[160:163], v[160:163], v[16:19], 0
	v_mfma_f32_16x16x32_bf16 v[160:163], v[164:167], v[12:15], v[160:163]
	s_nop 1
	v_cvt_pk_bf16_f32 v22, v152, v153
	v_cvt_pk_bf16_f32 v23, v154, v155
	global_store_dwordx2 v[20:21], v[22:23], off
	ds_read_b64_tr_b16 v[152:153], v59 offset:61056
	ds_read_b64_tr_b16 v[154:155], v59 offset:62144
	ds_read_b64_tr_b16 v[156:157], v133 offset:61056
	ds_read_b64_tr_b16 v[158:159], v133 offset:62144
	s_waitcnt lgkmcnt(8)
	v_mfma_f32_16x16x32_bf16 v[168:171], v[168:171], v[16:19], 0
	v_mfma_f32_16x16x32_bf16 v[168:171], v[172:175], v[12:15], v[168:171]
	s_nop 1
	v_cvt_pk_bf16_f32 v22, v160, v161
	v_cvt_pk_bf16_f32 v23, v162, v163
	global_store_dwordx2 v[20:21], v[22:23], off offset:32
	ds_read_b64_tr_b16 v[160:161], v59 offset:61088
	ds_read_b64_tr_b16 v[162:163], v59 offset:62176
	ds_read_b64_tr_b16 v[164:165], v133 offset:61088
	ds_read_b64_tr_b16 v[166:167], v133 offset:62176
	s_waitcnt lgkmcnt(8)
	v_mfma_f32_16x16x32_bf16 v[176:179], v[176:179], v[16:19], 0
	v_mfma_f32_16x16x32_bf16 v[176:179], v[180:183], v[12:15], v[176:179]
	s_nop 1
	v_cvt_pk_bf16_f32 v22, v168, v169
	v_cvt_pk_bf16_f32 v23, v170, v171
	global_store_dwordx2 v[20:21], v[22:23], off offset:64
	ds_read_b64_tr_b16 v[168:169], v59 offset:61120
	ds_read_b64_tr_b16 v[170:171], v59 offset:62208
	ds_read_b64_tr_b16 v[172:173], v133 offset:61120
	ds_read_b64_tr_b16 v[174:175], v133 offset:62208
	s_waitcnt lgkmcnt(8)
	v_mfma_f32_16x16x32_bf16 v[152:155], v[152:155], v[16:19], 0
	v_mfma_f32_16x16x32_bf16 v[152:155], v[156:159], v[12:15], v[152:155]
	s_nop 1
	v_cvt_pk_bf16_f32 v22, v176, v177
	v_cvt_pk_bf16_f32 v23, v178, v179
	global_store_dwordx2 v[20:21], v[22:23], off offset:96
	ds_read_b64_tr_b16 v[176:177], v59 offset:61152
	ds_read_b64_tr_b16 v[178:179], v59 offset:62240
	ds_read_b64_tr_b16 v[180:181], v133 offset:61152
	ds_read_b64_tr_b16 v[182:183], v133 offset:62240
	s_waitcnt lgkmcnt(8)
	v_mfma_f32_16x16x32_bf16 v[160:163], v[160:163], v[16:19], 0
	v_mfma_f32_16x16x32_bf16 v[160:163], v[164:167], v[12:15], v[160:163]
	s_nop 1
	v_cvt_pk_bf16_f32 v22, v152, v153
	v_cvt_pk_bf16_f32 v23, v154, v155
	global_store_dwordx2 v[20:21], v[22:23], off offset:128
	s_waitcnt lgkmcnt(4)
	v_mfma_f32_16x16x32_bf16 v[168:171], v[168:171], v[16:19], 0
	v_mfma_f32_16x16x32_bf16 v[168:171], v[172:175], v[12:15], v[168:171]
	s_nop 1
	v_cvt_pk_bf16_f32 v22, v160, v161
	v_cvt_pk_bf16_f32 v23, v162, v163
	global_store_dwordx2 v[20:21], v[22:23], off offset:160
	s_waitcnt lgkmcnt(0)
	v_mfma_f32_16x16x32_bf16 v[176:179], v[176:179], v[16:19], 0
	v_mfma_f32_16x16x32_bf16 v[176:179], v[180:183], v[12:15], v[176:179]
	s_nop 1
	v_cvt_pk_bf16_f32 v22, v168, v169
	v_cvt_pk_bf16_f32 v23, v170, v171
	global_store_dwordx2 v[20:21], v[22:23], off offset:192
	s_nop 7
	s_nop 1
	v_cvt_pk_bf16_f32 v22, v176, v177
	v_cvt_pk_bf16_f32 v23, v178, v179
	global_store_dwordx2 v[20:21], v[22:23], off offset:224
	s_waitcnt lgkmcnt(0)
	s_barrier
	s_cbranch_vccnz .LBB0_648
